# v14: v10 + phase-10 end-of-round waits no longer drain the round's 24 mix stores (counts +24 on the fall-through path)
# speedup vs baseline: 1.0143x; 1.0143x over previous
.LBB0_1138:
	s_mul_hi_u32 s0, s36, 0xcccccccd
	s_lshr_b32 s0, s0, 4
	s_mul_i32 s0, s0, 0x14000
	v_subrev_u32_e32 v3, s0, v53
	s_mul_hi_u32 s0, s45, 0xcccccccd
	s_lshr_b32 s0, s0, 4
	s_cmp_gt_i32 s20, 0
	s_mul_i32 s0, s0, 0x14000
	s_cselect_b64 s[4:5], -1, 0
	s_cmp_lt_i32 s20, s23
	s_waitcnt vmcnt(16)
	v_subrev_u32_e32 v4, s0, v142
	s_cselect_b64 vcc, -1, 0
	s_add_i32 s20, s44, s48
	v_add_u32_e32 v94, s20, v3
	v_add_u32_e32 v3, s20, v4
	v_add_u32_e32 v95, s20, v2
	ds_read_b128 v[14:17], v94
	ds_read_b128 v[10:13], v3
	ds_read_b128 v[6:9], v95
	ds_read_b128 v[2:5], v94 offset:1024
	v_cndmask_b32_e64 v92, 0, 0.5, vcc
	v_cndmask_b32_e64 v54, 0, 0.5, s[4:5]
	s_ashr_i32 s23, s22, 31
	s_waitcnt lgkmcnt(1)
	v_lshlrev_b32_e32 v90, 16, v6
	v_and_b32_e32 v6, 0xffff0000, v6
	v_lshlrev_b32_e32 v97, 16, v14
	v_and_b32_e32 v98, 0xffff0000, v14
	v_lshlrev_b32_e32 v14, 16, v10
	v_and_b32_e32 v10, 0xffff0000, v10
	v_cndmask_b32_e32 v6, 0, v6, vcc
	v_cndmask_b32_e64 v10, 0, v10, s[4:5]
	v_mul_f32_e32 v6, v92, v6
	v_fmac_f32_e32 v6, v54, v10
	v_sub_f32_e32 v100, v6, v98
	v_lshlrev_b32_e32 v6, 16, v11
	v_and_b32_e32 v10, 0xffff0000, v11
	v_lshlrev_b32_e32 v11, 16, v7
	v_cndmask_b32_e32 v11, 0, v11, vcc
	v_and_b32_e32 v7, 0xffff0000, v7
	v_cndmask_b32_e64 v6, 0, v6, s[4:5]
	v_cndmask_b32_e32 v7, 0, v7, vcc
	v_mul_f32_e32 v11, v92, v11
	v_cndmask_b32_e64 v10, 0, v10, s[4:5]
	v_fmac_f32_e32 v11, v54, v6
	v_mul_f32_e32 v6, v92, v7
	v_and_b32_e32 v102, 0xffff0000, v15
	v_fmac_f32_e32 v6, v54, v10
	v_lshlrev_b32_e32 v10, 16, v8
	v_sub_f32_e32 v104, v6, v102
	v_lshlrev_b32_e32 v6, 16, v12
	v_cndmask_b32_e32 v10, 0, v10, vcc
	v_and_b32_e32 v8, 0xffff0000, v8
	v_cndmask_b32_e64 v6, 0, v6, s[4:5]
	v_and_b32_e32 v7, 0xffff0000, v12
	v_cndmask_b32_e32 v8, 0, v8, vcc
	v_mul_f32_e32 v10, v92, v10
	v_cndmask_b32_e64 v7, 0, v7, s[4:5]
	v_fmac_f32_e32 v10, v54, v6
	v_mul_f32_e32 v6, v92, v8
	v_lshlrev_b32_e32 v105, 16, v16
	v_fmac_f32_e32 v6, v54, v7
	v_and_b32_e32 v7, 0xffff0000, v13
	v_and_b32_e32 v16, 0xffff0000, v16
	v_sub_f32_e32 v106, v10, v105
	v_cndmask_b32_e64 v10, 0, v7, s[4:5]
	v_lshlrev_b32_e32 v7, 16, v9
	v_sub_f32_e32 v107, v6, v16
	v_lshlrev_b32_e32 v6, 16, v13
	v_cndmask_b32_e32 v7, 0, v7, vcc
	v_lshlrev_b32_e32 v101, 16, v15
	v_cndmask_b32_e64 v6, 0, v6, s[4:5]
	v_and_b32_e32 v8, 0xffff0000, v9
	v_mul_f32_e32 v7, v92, v7
	v_sub_f32_e32 v103, v11, v101
	v_lshlrev_b32_e32 v108, 16, v17
	v_cndmask_b32_e32 v11, 0, v8, vcc
	v_fmac_f32_e32 v7, v54, v6
	v_sub_f32_e32 v109, v7, v108
	ds_read_b128 v[6:9], v136 offset:8192
	v_mul_f32_e32 v11, v92, v11
	v_cndmask_b32_e32 v90, 0, v90, vcc
	v_and_b32_e32 v17, 0xffff0000, v17
	v_fmac_f32_e32 v11, v54, v10
	v_cndmask_b32_e64 v14, 0, v14, s[4:5]
	v_mul_f32_e32 v90, v92, v90
	v_sub_f32_e32 v110, v11, v17
	ds_read_b128 v[10:13], v136 offset:8208
	v_fmac_f32_e32 v90, v54, v14
	v_sub_f32_e32 v99, v90, v97
	s_waitcnt lgkmcnt(1)
	v_fma_f32 v6, v6, v99, v97
	v_fma_f32 v7, v7, v100, v98
	v_cvt_pk_bf16_f32 v6, v6, v7
	v_fma_f32 v7, v8, v103, v101
	v_fma_f32 v8, v9, v104, v102
	v_cvt_pk_bf16_f32 v7, v7, v8
	s_waitcnt lgkmcnt(0)
	v_fma_f32 v8, v10, v106, v105
	v_fma_f32 v9, v11, v107, v16
	s_lshl_b64 s[22:23], s[22:23], 12
	v_cvt_pk_bf16_f32 v8, v8, v9
	v_fma_f32 v9, v12, v109, v108
	v_fma_f32 v14, v13, v110, v17
	ds_read_b128 v[10:13], v136 offset:32768
	v_cvt_pk_bf16_f32 v9, v9, v14
	v_lshl_add_u64 v[90:91], v[70:71], 0, s[22:23]
	global_store_dwordx4 v[90:91], v[6:9], off
	ds_read_b128 v[6:9], v136 offset:32784
	s_waitcnt lgkmcnt(1)
	v_fma_f32 v10, v10, v99, v97
	v_fma_f32 v11, v11, v100, v98
	v_cvt_pk_bf16_f32 v10, v10, v11
	v_fma_f32 v11, v12, v103, v101
	v_fma_f32 v12, v13, v104, v102
	s_waitcnt lgkmcnt(0)
	v_fma_f32 v6, v6, v106, v105
	v_fma_f32 v7, v7, v107, v16
	v_cvt_pk_bf16_f32 v11, v11, v12
	v_cvt_pk_bf16_f32 v12, v6, v7
	v_fma_f32 v13, v8, v109, v108
	v_fma_f32 v14, v9, v110, v17
	ds_read_b128 v[6:9], v136 offset:40960
	v_cvt_pk_bf16_f32 v13, v13, v14
	v_lshl_add_u64 v[14:15], v[56:57], 0, s[22:23]
	global_store_dwordx4 v[14:15], v[10:13], off
	ds_read_b128 v[10:13], v136 offset:40976
	s_waitcnt lgkmcnt(1)
	v_fma_f32 v6, v99, v6, v97
	v_fma_f32 v7, v100, v7, v98
	v_cvt_pk_bf16_f32 v6, v6, v7
	v_fma_f32 v7, v103, v8, v101
	v_fma_f32 v8, v104, v9, v102
	v_cvt_pk_bf16_f32 v7, v7, v8
	s_waitcnt lgkmcnt(0)
	v_fma_f32 v8, v106, v10, v105
	v_fma_f32 v9, v107, v11, v16
	v_cvt_pk_bf16_f32 v8, v8, v9
	v_fma_f32 v9, v109, v12, v108
	v_fma_f32 v14, v110, v13, v17
	ds_read_b128 v[10:13], v136
	v_cvt_pk_bf16_f32 v9, v9, v14
	v_lshl_add_u64 v[14:15], v[58:59], 0, s[22:23]
	global_store_dwordx4 v[14:15], v[6:9], off
	ds_read_b128 v[6:9], v136 offset:16
	s_waitcnt lgkmcnt(1)
	v_fma_f32 v10, v99, v10, v97
	v_fma_f32 v11, v100, v11, v98
	v_cvt_pk_bf16_f32 v10, v10, v11
	v_fma_f32 v11, v103, v12, v101
	v_fma_f32 v12, v104, v13, v102
	s_waitcnt lgkmcnt(0)
	v_fma_f32 v6, v106, v6, v105
	v_fma_f32 v7, v107, v7, v16
	v_cvt_pk_bf16_f32 v11, v11, v12
	v_cvt_pk_bf16_f32 v12, v6, v7
	v_fma_f32 v13, v109, v8, v108
	v_fma_f32 v14, v110, v9, v17
	ds_read_b128 v[6:9], v136 offset:16384
	v_cvt_pk_bf16_f32 v13, v13, v14
	v_lshl_add_u64 v[14:15], v[60:61], 0, s[22:23]
	global_store_dwordx4 v[14:15], v[10:13], off
	ds_read_b128 v[10:13], v136 offset:16400
	s_waitcnt lgkmcnt(1)
	v_fma_f32 v6, v99, v6, v97
	v_fma_f32 v7, v100, v7, v98
	v_cvt_pk_bf16_f32 v6, v6, v7
	v_fma_f32 v7, v103, v8, v101
	v_fma_f32 v8, v104, v9, v102
	v_cvt_pk_bf16_f32 v7, v7, v8
	s_waitcnt lgkmcnt(0)
	v_fma_f32 v8, v106, v10, v105
	v_fma_f32 v9, v107, v11, v16
	v_cvt_pk_bf16_f32 v8, v8, v9
	v_fma_f32 v9, v109, v12, v108
	v_fma_f32 v14, v110, v13, v17
	v_cvt_pk_bf16_f32 v9, v9, v14
	v_lshl_add_u64 v[14:15], v[62:63], 0, s[22:23]
	ds_read_b128 v[10:13], v136 offset:24576
	global_store_dwordx4 v[14:15], v[6:9], off
	ds_read_b128 v[6:9], v136 offset:24592
	v_subrev_u32_e32 v96, s0, v141
	v_lshlrev_b32_e32 v149, 16, v5
	s_waitcnt lgkmcnt(1)
	v_fmac_f32_e32 v97, v99, v10
	v_fmac_f32_e32 v98, v100, v11
	v_fmac_f32_e32 v101, v103, v12
	v_fmac_f32_e32 v102, v104, v13
	s_waitcnt lgkmcnt(0)
	v_fmac_f32_e32 v105, v106, v6
	v_fmac_f32_e32 v16, v107, v7
	v_fmac_f32_e32 v108, v109, v8
	v_fmac_f32_e32 v17, v110, v9
	v_cvt_pk_bf16_f32 v10, v97, v98
	v_cvt_pk_bf16_f32 v11, v101, v102
	v_cvt_pk_bf16_f32 v12, v105, v16
	v_cvt_pk_bf16_f32 v13, v108, v17
	v_lshl_add_u64 v[6:7], v[64:65], 0, s[22:23]
	global_store_dwordx4 v[6:7], v[10:13], off
	v_add_u32_e32 v6, s20, v96
	ds_read_b128 v[10:13], v6
	ds_read_b128 v[6:9], v95 offset:1024
	ds_read_b128 v[14:17], v95 offset:3072
	ds_read_b128 v[98:101], v95 offset:2048
	v_lshlrev_b32_e32 v96, 16, v2
	s_waitcnt lgkmcnt(3)
	v_lshlrev_b32_e32 v97, 16, v10
	s_waitcnt lgkmcnt(2)
	v_lshlrev_b32_e32 v95, 16, v6
	v_and_b32_e32 v6, 0xffff0000, v6
	v_and_b32_e32 v10, 0xffff0000, v10
	v_cndmask_b32_e32 v6, 0, v6, vcc
	v_cndmask_b32_e64 v10, 0, v10, s[4:5]
	v_cndmask_b32_e32 v95, 0, v95, vcc
	v_mul_f32_e32 v6, v92, v6
	v_and_b32_e32 v2, 0xffff0000, v2
	v_cndmask_b32_e64 v97, 0, v97, s[4:5]
	v_mul_f32_e32 v95, v92, v95
	v_fmac_f32_e32 v6, v54, v10
	v_fmac_f32_e32 v95, v54, v97
	v_sub_f32_e32 v97, v6, v2
	v_lshlrev_b32_e32 v6, 16, v11
	v_and_b32_e32 v10, 0xffff0000, v11
	v_lshlrev_b32_e32 v11, 16, v7
	v_cndmask_b32_e32 v11, 0, v11, vcc
	v_and_b32_e32 v7, 0xffff0000, v7
	v_cndmask_b32_e64 v6, 0, v6, s[4:5]
	v_cndmask_b32_e32 v7, 0, v7, vcc
	v_mul_f32_e32 v11, v92, v11
	v_cndmask_b32_e64 v10, 0, v10, s[4:5]
	v_fmac_f32_e32 v11, v54, v6
	v_mul_f32_e32 v6, v92, v7
	v_lshlrev_b32_e32 v7, 16, v8
	v_lshlrev_b32_e32 v106, 16, v3
	v_and_b32_e32 v3, 0xffff0000, v3
	v_fmac_f32_e32 v6, v54, v10
	v_lshlrev_b32_e32 v109, 16, v4
	v_and_b32_e32 v110, 0xffff0000, v4
	v_lshlrev_b32_e32 v4, 16, v12
	v_cndmask_b32_e32 v7, 0, v7, vcc
	v_and_b32_e32 v8, 0xffff0000, v8
	v_sub_f32_e32 v108, v6, v3
	v_cndmask_b32_e64 v4, 0, v4, s[4:5]
	v_and_b32_e32 v6, 0xffff0000, v12
	v_cndmask_b32_e32 v8, 0, v8, vcc
	v_mul_f32_e32 v7, v92, v7
	v_cndmask_b32_e64 v6, 0, v6, s[4:5]
	v_fmac_f32_e32 v7, v54, v4
	v_mul_f32_e32 v4, v92, v8
	v_and_b32_e32 v150, 0xffff0000, v5
	v_and_b32_e32 v5, 0xffff0000, v13
	v_fmac_f32_e32 v4, v54, v6
	v_cndmask_b32_e64 v8, 0, v5, s[4:5]
	v_lshlrev_b32_e32 v5, 16, v9
	v_sub_f32_e32 v111, v4, v110
	v_lshlrev_b32_e32 v4, 16, v13
	v_cndmask_b32_e32 v5, 0, v5, vcc
	v_cndmask_b32_e64 v4, 0, v4, s[4:5]
	v_and_b32_e32 v6, 0xffff0000, v9
	v_mul_f32_e32 v5, v92, v5
	v_cndmask_b32_e32 v9, 0, v6, vcc
	v_fmac_f32_e32 v5, v54, v4
	v_sub_f32_e32 v12, v7, v109
	v_sub_f32_e32 v13, v5, v149
	ds_read_b128 v[4:7], v137 offset:8192
	v_mul_f32_e32 v9, v92, v9
	v_fmac_f32_e32 v9, v54, v8
	v_sub_f32_e32 v107, v11, v106
	v_sub_f32_e32 v151, v9, v150
	ds_read_b128 v[8:11], v137 offset:8208
	v_sub_f32_e32 v95, v95, v96
	s_waitcnt lgkmcnt(1)
	v_fma_f32 v4, v4, v95, v96
	v_fma_f32 v5, v5, v97, v2
	v_cvt_pk_bf16_f32 v4, v4, v5
	v_fma_f32 v5, v6, v107, v106
	v_fma_f32 v6, v7, v108, v3
	v_cvt_pk_bf16_f32 v5, v5, v6
	s_waitcnt lgkmcnt(0)
	v_fma_f32 v6, v8, v12, v109
	v_fma_f32 v7, v9, v111, v110
	v_cvt_pk_bf16_f32 v6, v6, v7
	v_fma_f32 v7, v10, v13, v149
	v_fma_f32 v8, v11, v151, v150
	ds_read_b128 v[102:105], v137 offset:32768
	v_cvt_pk_bf16_f32 v7, v7, v8
	global_store_dwordx4 v[90:91], v[4:7], off offset:1024
	ds_read_b128 v[4:7], v137 offset:32784
	s_add_u32 s30, s10, s22
	s_waitcnt lgkmcnt(1)
	v_fma_f32 v8, v102, v95, v96
	v_fma_f32 v9, v103, v97, v2
	v_cvt_pk_bf16_f32 v8, v8, v9
	v_fma_f32 v9, v104, v107, v106
	v_fma_f32 v10, v105, v108, v3
	s_waitcnt lgkmcnt(0)
	v_fma_f32 v4, v4, v12, v109
	v_fma_f32 v5, v5, v111, v110
	v_cvt_pk_bf16_f32 v9, v9, v10
	v_cvt_pk_bf16_f32 v10, v4, v5
	v_fma_f32 v4, v6, v13, v149
	v_fma_f32 v5, v7, v151, v150
	v_cvt_pk_bf16_f32 v11, v4, v5
	ds_read_b128 v[4:7], v137 offset:40960
	s_addc_u32 s31, s11, s23
	global_store_dwordx4 v144, v[8:11], s[30:31]
	ds_read_b128 v[8:11], v137 offset:40976
	s_add_u32 s28, s12, s22
	s_waitcnt lgkmcnt(1)
	v_fma_f32 v4, v95, v4, v96
	v_fma_f32 v5, v97, v5, v2
	v_cvt_pk_bf16_f32 v4, v4, v5
	v_fma_f32 v5, v107, v6, v106
	v_fma_f32 v6, v108, v7, v3
	v_cvt_pk_bf16_f32 v5, v5, v6
	s_waitcnt lgkmcnt(0)
	v_fma_f32 v6, v12, v8, v109
	v_fma_f32 v7, v111, v9, v110
	v_cvt_pk_bf16_f32 v6, v6, v7
	v_fma_f32 v7, v13, v10, v149
	v_fma_f32 v8, v151, v11, v150
	v_cvt_pk_bf16_f32 v7, v7, v8
	ds_read_b128 v[8:11], v137
	s_addc_u32 s29, s13, s23
	global_store_dwordx4 v144, v[4:7], s[28:29]
	ds_read_b128 v[4:7], v137 offset:16
	s_add_u32 s26, s14, s22
	s_waitcnt lgkmcnt(1)
	v_fma_f32 v8, v95, v8, v96
	v_fma_f32 v9, v97, v9, v2
	v_cvt_pk_bf16_f32 v8, v8, v9
	v_fma_f32 v9, v107, v10, v106
	v_fma_f32 v10, v108, v11, v3
	s_waitcnt lgkmcnt(0)
	v_fma_f32 v4, v12, v4, v109
	v_fma_f32 v5, v111, v5, v110
	v_cvt_pk_bf16_f32 v9, v9, v10
	v_cvt_pk_bf16_f32 v10, v4, v5
	v_fma_f32 v4, v13, v6, v149
	v_fma_f32 v5, v151, v7, v150
	v_cvt_pk_bf16_f32 v11, v4, v5
	ds_read_b128 v[4:7], v137 offset:16384
	s_addc_u32 s27, s15, s23
	global_store_dwordx4 v144, v[8:11], s[26:27]
	ds_read_b128 v[8:11], v137 offset:16400
	s_add_u32 s24, s16, s22
	s_waitcnt lgkmcnt(1)
	v_fma_f32 v4, v95, v4, v96
	v_fma_f32 v5, v97, v5, v2
	v_cvt_pk_bf16_f32 v4, v4, v5
	v_fma_f32 v5, v107, v6, v106
	v_fma_f32 v6, v108, v7, v3
	v_cvt_pk_bf16_f32 v5, v5, v6
	s_waitcnt lgkmcnt(0)
	v_fma_f32 v6, v12, v8, v109
	v_fma_f32 v7, v111, v9, v110
	v_cvt_pk_bf16_f32 v6, v6, v7
	v_fma_f32 v7, v13, v10, v149
	v_fma_f32 v8, v151, v11, v150
	v_cvt_pk_bf16_f32 v7, v7, v8
	s_addc_u32 s25, s17, s23
	ds_read_b128 v[8:11], v137 offset:24576
	global_store_dwordx4 v144, v[4:7], s[24:25]
	ds_read_b128 v[4:7], v137 offset:24592
	s_add_u32 s22, s18, s22
	v_subrev_u32_e32 v93, s0, v140
	s_waitcnt lgkmcnt(1)
	v_fmac_f32_e32 v96, v95, v8
	v_fmac_f32_e32 v2, v97, v9
	v_fmac_f32_e32 v106, v107, v10
	v_fmac_f32_e32 v3, v108, v11
	s_waitcnt lgkmcnt(0)
	v_fmac_f32_e32 v109, v12, v4
	v_fmac_f32_e32 v110, v111, v5
	v_fmac_f32_e32 v149, v13, v6
	v_fmac_f32_e32 v150, v151, v7
	v_cvt_pk_bf16_f32 v2, v96, v2
	v_cvt_pk_bf16_f32 v3, v106, v3
	v_cvt_pk_bf16_f32 v4, v109, v110
	v_cvt_pk_bf16_f32 v5, v149, v150
	s_addc_u32 s23, s19, s23
	ds_read_b128 v[6:9], v94 offset:2048
	global_store_dwordx4 v144, v[2:5], s[22:23]
	v_add_u32_e32 v93, s20, v93
	ds_read_b128 v[2:5], v93
	ds_read_b128 v[10:13], v94 offset:3072
	ds_read_b128 v[94:97], v93 offset:1024
	v_lshlrev_b32_e32 v93, 16, v98
	s_waitcnt lgkmcnt(3)
	v_lshlrev_b32_e32 v102, 16, v6
	v_and_b32_e32 v103, 0xffff0000, v6
	s_waitcnt lgkmcnt(2)
	v_lshlrev_b32_e32 v6, 16, v2
	v_cndmask_b32_e32 v93, 0, v93, vcc
	v_and_b32_e32 v98, 0xffff0000, v98
	v_cndmask_b32_e64 v6, 0, v6, s[4:5]
	v_and_b32_e32 v2, 0xffff0000, v2
	v_cndmask_b32_e32 v98, 0, v98, vcc
	v_mul_f32_e32 v93, v92, v93
	v_cndmask_b32_e64 v2, 0, v2, s[4:5]
	v_fmac_f32_e32 v93, v54, v6
	v_mul_f32_e32 v6, v92, v98
	v_fmac_f32_e32 v6, v54, v2
	v_sub_f32_e32 v104, v6, v103
	v_lshlrev_b32_e32 v6, 16, v99
	v_lshlrev_b32_e32 v105, 16, v7
	v_and_b32_e32 v106, 0xffff0000, v7
	v_lshlrev_b32_e32 v2, 16, v3
	v_cndmask_b32_e32 v6, 0, v6, vcc
	v_and_b32_e32 v7, 0xffff0000, v99
	v_cndmask_b32_e64 v2, 0, v2, s[4:5]
	v_and_b32_e32 v3, 0xffff0000, v3
	v_cndmask_b32_e32 v7, 0, v7, vcc
	v_mul_f32_e32 v6, v92, v6
	v_cndmask_b32_e64 v3, 0, v3, s[4:5]
	v_fmac_f32_e32 v6, v54, v2
	v_mul_f32_e32 v2, v92, v7
	v_fmac_f32_e32 v2, v54, v3
	v_sub_f32_e32 v108, v2, v106
	v_lshlrev_b32_e32 v2, 16, v4
	v_and_b32_e32 v3, 0xffff0000, v4
	v_lshlrev_b32_e32 v4, 16, v100
	v_sub_f32_e32 v107, v6, v105
	v_cndmask_b32_e32 v4, 0, v4, vcc
	v_and_b32_e32 v6, 0xffff0000, v100
	v_cndmask_b32_e64 v2, 0, v2, s[4:5]
	v_cndmask_b32_e32 v6, 0, v6, vcc
	v_mul_f32_e32 v4, v92, v4
	v_cndmask_b32_e64 v3, 0, v3, s[4:5]
	v_fmac_f32_e32 v4, v54, v2
	v_mul_f32_e32 v2, v92, v6
	v_fmac_f32_e32 v2, v54, v3
	v_and_b32_e32 v3, 0xffff0000, v5
	v_and_b32_e32 v110, 0xffff0000, v8
	v_cndmask_b32_e64 v6, 0, v3, s[4:5]
	v_lshlrev_b32_e32 v3, 16, v101
	v_lshlrev_b32_e32 v109, 16, v8
	v_sub_f32_e32 v149, v2, v110
	v_lshlrev_b32_e32 v2, 16, v5
	v_cndmask_b32_e32 v3, 0, v3, vcc
	v_sub_f32_e32 v111, v4, v109
	v_cndmask_b32_e64 v2, 0, v2, s[4:5]
	v_and_b32_e32 v4, 0xffff0000, v101
	v_mul_f32_e32 v3, v92, v3
	v_lshlrev_b32_e32 v150, 16, v9
	v_cndmask_b32_e32 v7, 0, v4, vcc
	v_fmac_f32_e32 v3, v54, v2
	v_sub_f32_e32 v152, v3, v150
	ds_read_b128 v[2:5], v138 offset:8192
	v_mul_f32_e32 v7, v92, v7
	v_and_b32_e32 v151, 0xffff0000, v9
	v_fmac_f32_e32 v7, v54, v6
	v_sub_f32_e32 v153, v7, v151
	ds_read_b128 v[6:9], v138 offset:8208
	v_sub_f32_e32 v93, v93, v102
	s_waitcnt lgkmcnt(1)
	v_fma_f32 v2, v2, v93, v102
	v_fma_f32 v3, v3, v104, v103
	v_cvt_pk_bf16_f32 v2, v2, v3
	v_fma_f32 v3, v4, v107, v105
	v_fma_f32 v4, v5, v108, v106
	v_cvt_pk_bf16_f32 v3, v3, v4
	s_waitcnt lgkmcnt(0)
	v_fma_f32 v4, v6, v111, v109
	v_fma_f32 v5, v7, v149, v110
	v_cvt_pk_bf16_f32 v4, v4, v5
	v_fma_f32 v5, v8, v152, v150
	v_fma_f32 v6, v9, v153, v151
	ds_read_b128 v[98:101], v138 offset:32768
	v_cvt_pk_bf16_f32 v5, v5, v6
	global_store_dwordx4 v[90:91], v[2:5], off offset:2048
	ds_read_b128 v[2:5], v138 offset:32784
	s_waitcnt lgkmcnt(1)
	v_fma_f32 v6, v98, v93, v102
	v_fma_f32 v7, v99, v104, v103
	v_cvt_pk_bf16_f32 v6, v6, v7
	v_fma_f32 v7, v100, v107, v105
	v_fma_f32 v8, v101, v108, v106
	s_waitcnt lgkmcnt(0)
	v_fma_f32 v2, v2, v111, v109
	v_fma_f32 v3, v3, v149, v110
	v_cvt_pk_bf16_f32 v7, v7, v8
	v_cvt_pk_bf16_f32 v8, v2, v3
	v_fma_f32 v2, v4, v152, v150
	ds_read_b128 v[98:101], v138 offset:40960
	v_fma_f32 v3, v5, v153, v151
	v_cvt_pk_bf16_f32 v9, v2, v3
	ds_read_b128 v[2:5], v138 offset:40976
	global_store_dwordx4 v145, v[6:9], s[30:31]
	s_waitcnt lgkmcnt(0)
	v_fma_f32 v2, v111, v2, v109
	v_fma_f32 v6, v93, v98, v102
	v_fma_f32 v7, v104, v99, v103
	v_cvt_pk_bf16_f32 v6, v6, v7
	v_fma_f32 v7, v107, v100, v105
	v_fma_f32 v8, v108, v101, v106
	v_fma_f32 v3, v149, v3, v110
	v_cvt_pk_bf16_f32 v7, v7, v8
	v_cvt_pk_bf16_f32 v8, v2, v3
	v_fma_f32 v2, v152, v4, v150
	ds_read_b128 v[98:101], v138
	v_fma_f32 v3, v153, v5, v151
	v_cvt_pk_bf16_f32 v9, v2, v3
	ds_read_b128 v[2:5], v138 offset:16
	global_store_dwordx4 v145, v[6:9], s[28:29]
	s_waitcnt lgkmcnt(0)
	v_fma_f32 v2, v111, v2, v109
	v_fma_f32 v6, v93, v98, v102
	v_fma_f32 v7, v104, v99, v103
	v_cvt_pk_bf16_f32 v6, v6, v7
	v_fma_f32 v7, v107, v100, v105
	v_fma_f32 v8, v108, v101, v106
	v_fma_f32 v3, v149, v3, v110
	v_cvt_pk_bf16_f32 v7, v7, v8
	v_cvt_pk_bf16_f32 v8, v2, v3
	v_fma_f32 v2, v152, v4, v150
	ds_read_b128 v[98:101], v138 offset:16384
	v_fma_f32 v3, v153, v5, v151
	v_cvt_pk_bf16_f32 v9, v2, v3
	ds_read_b128 v[2:5], v138 offset:16400
	global_store_dwordx4 v145, v[6:9], s[26:27]
	s_waitcnt lgkmcnt(0)
	v_fma_f32 v2, v111, v2, v109
	v_fma_f32 v6, v93, v98, v102
	v_fma_f32 v7, v104, v99, v103
	v_cvt_pk_bf16_f32 v6, v6, v7
	v_fma_f32 v7, v107, v100, v105
	v_fma_f32 v8, v108, v101, v106
	v_fma_f32 v3, v149, v3, v110
	v_cvt_pk_bf16_f32 v7, v7, v8
	v_cvt_pk_bf16_f32 v8, v2, v3
	v_fma_f32 v2, v152, v4, v150
	v_fma_f32 v3, v153, v5, v151
	ds_read_b128 v[98:101], v138 offset:24576
	v_cvt_pk_bf16_f32 v9, v2, v3
	ds_read_b128 v[2:5], v138 offset:24592
	global_store_dwordx4 v145, v[6:9], s[24:25]
	s_waitcnt lgkmcnt(1)
	v_fmac_f32_e32 v102, v93, v98
	v_lshlrev_b32_e32 v93, 16, v10
	s_waitcnt lgkmcnt(0)
	v_fmac_f32_e32 v150, v152, v4
	v_lshlrev_b32_e32 v4, 16, v14
	v_fmac_f32_e32 v109, v111, v2
	v_fmac_f32_e32 v151, v153, v5
	v_lshlrev_b32_e32 v2, 16, v94
	v_cndmask_b32_e32 v4, 0, v4, vcc
	v_and_b32_e32 v5, 0xffff0000, v14
	v_fmac_f32_e32 v110, v149, v3
	v_cndmask_b32_e64 v2, 0, v2, s[4:5]
	v_and_b32_e32 v3, 0xffff0000, v94
	v_cndmask_b32_e32 v5, 0, v5, vcc
	v_mul_f32_e32 v4, v92, v4
	v_cndmask_b32_e64 v3, 0, v3, s[4:5]
	v_fmac_f32_e32 v4, v54, v2
	v_mul_f32_e32 v2, v92, v5
	v_and_b32_e32 v98, 0xffff0000, v10
	v_sub_f32_e32 v14, v4, v93
	v_fmac_f32_e32 v2, v54, v3
	v_lshlrev_b32_e32 v4, 16, v15
	v_sub_f32_e32 v94, v2, v98
	v_lshlrev_b32_e32 v2, 16, v95
	v_cndmask_b32_e32 v4, 0, v4, vcc
	v_and_b32_e32 v5, 0xffff0000, v15
	v_cndmask_b32_e64 v2, 0, v2, s[4:5]
	v_and_b32_e32 v3, 0xffff0000, v95
	v_cndmask_b32_e32 v5, 0, v5, vcc
	v_mul_f32_e32 v4, v92, v4
	v_fmac_f32_e32 v103, v104, v99
	v_lshlrev_b32_e32 v99, 16, v11
	v_cndmask_b32_e64 v3, 0, v3, s[4:5]
	v_fmac_f32_e32 v4, v54, v2
	v_mul_f32_e32 v2, v92, v5
	v_fmac_f32_e32 v105, v107, v100
	v_and_b32_e32 v100, 0xffff0000, v11
	v_sub_f32_e32 v15, v4, v99
	v_fmac_f32_e32 v2, v54, v3
	v_lshlrev_b32_e32 v4, 16, v16
	v_sub_f32_e32 v95, v2, v100
	v_lshlrev_b32_e32 v2, 16, v96
	v_cndmask_b32_e32 v4, 0, v4, vcc
	v_and_b32_e32 v5, 0xffff0000, v16
	v_cndmask_b32_e64 v2, 0, v2, s[4:5]
	v_and_b32_e32 v3, 0xffff0000, v96
	v_cndmask_b32_e32 v5, 0, v5, vcc
	v_mul_f32_e32 v4, v92, v4
	v_fmac_f32_e32 v106, v108, v101
	v_cndmask_b32_e64 v3, 0, v3, s[4:5]
	v_fmac_f32_e32 v4, v54, v2
	v_mul_f32_e32 v2, v92, v5
	v_cvt_pk_bf16_f32 v6, v102, v103
	v_cvt_pk_bf16_f32 v7, v105, v106
	v_cvt_pk_bf16_f32 v8, v109, v110
	v_cvt_pk_bf16_f32 v9, v150, v151
	v_fmac_f32_e32 v2, v54, v3
	v_and_b32_e32 v3, 0xffff0000, v97
	global_store_dwordx4 v145, v[6:9], s[22:23]
	v_and_b32_e32 v102, 0xffff0000, v12
	v_lshlrev_b32_e32 v101, 16, v12
	v_cndmask_b32_e64 v6, 0, v3, s[4:5]
	v_lshlrev_b32_e32 v3, 16, v17
	v_sub_f32_e32 v96, v2, v102
	v_lshlrev_b32_e32 v2, 16, v97
	v_cndmask_b32_e32 v3, 0, v3, vcc
	v_sub_f32_e32 v16, v4, v101
	v_cndmask_b32_e64 v2, 0, v2, s[4:5]
	v_and_b32_e32 v4, 0xffff0000, v17
	v_mul_f32_e32 v3, v92, v3
	v_lshlrev_b32_e32 v103, 16, v13
	v_cndmask_b32_e32 v7, 0, v4, vcc
	v_fmac_f32_e32 v3, v54, v2
	v_sub_f32_e32 v17, v3, v103
	ds_read_b128 v[2:5], v139 offset:8192
	v_mul_f32_e32 v7, v92, v7
	v_and_b32_e32 v104, 0xffff0000, v13
	v_fmac_f32_e32 v7, v54, v6
	v_sub_f32_e32 v54, v7, v104
	ds_read_b128 v[6:9], v139 offset:8208
	s_waitcnt lgkmcnt(1)
	v_fma_f32 v2, v2, v14, v93
	v_fma_f32 v3, v3, v94, v98
	v_cvt_pk_bf16_f32 v2, v2, v3
	v_fma_f32 v3, v4, v15, v99
	v_fma_f32 v4, v5, v95, v100
	v_cvt_pk_bf16_f32 v3, v3, v4
	s_waitcnt lgkmcnt(0)
	v_fma_f32 v4, v6, v16, v101
	v_fma_f32 v5, v7, v96, v102
	v_cvt_pk_bf16_f32 v4, v4, v5
	v_fma_f32 v5, v8, v17, v103
	v_fma_f32 v6, v9, v54, v104
	ds_read_b128 v[10:13], v139 offset:32768
	v_cvt_pk_bf16_f32 v5, v5, v6
	global_store_dwordx4 v[90:91], v[2:5], off offset:3072
	ds_read_b128 v[2:5], v139 offset:32784
	s_waitcnt lgkmcnt(1)
	v_fma_f32 v6, v10, v14, v93
	v_fma_f32 v7, v11, v94, v98
	v_cvt_pk_bf16_f32 v6, v6, v7
	v_fma_f32 v7, v12, v15, v99
	v_fma_f32 v8, v13, v95, v100
	s_waitcnt lgkmcnt(0)
	v_fma_f32 v2, v2, v16, v101
	v_fma_f32 v3, v3, v96, v102
	v_cvt_pk_bf16_f32 v7, v7, v8
	v_cvt_pk_bf16_f32 v8, v2, v3
	v_fma_f32 v2, v4, v17, v103
	ds_read_b128 v[10:13], v139 offset:40960
	v_fma_f32 v3, v5, v54, v104
	v_cvt_pk_bf16_f32 v9, v2, v3
	ds_read_b128 v[2:5], v139 offset:40976
	global_store_dwordx4 v146, v[6:9], s[30:31]
	s_waitcnt lgkmcnt(0)
	v_fma_f32 v2, v16, v2, v101
	v_fma_f32 v6, v14, v10, v93
	v_fma_f32 v7, v94, v11, v98
	v_cvt_pk_bf16_f32 v6, v6, v7
	v_fma_f32 v7, v15, v12, v99
	v_fma_f32 v8, v95, v13, v100
	v_fma_f32 v3, v96, v3, v102
	v_cvt_pk_bf16_f32 v7, v7, v8
	v_cvt_pk_bf16_f32 v8, v2, v3
	v_fma_f32 v2, v17, v4, v103
	ds_read_b128 v[10:13], v139
	v_fma_f32 v3, v54, v5, v104
	v_cvt_pk_bf16_f32 v9, v2, v3
	ds_read_b128 v[2:5], v139 offset:16
	global_store_dwordx4 v146, v[6:9], s[28:29]
	s_waitcnt lgkmcnt(0)
	v_fma_f32 v2, v16, v2, v101
	v_fma_f32 v6, v14, v10, v93
	v_fma_f32 v7, v94, v11, v98
	v_cvt_pk_bf16_f32 v6, v6, v7
	v_fma_f32 v7, v15, v12, v99
	v_fma_f32 v8, v95, v13, v100
	v_fma_f32 v3, v96, v3, v102
	v_cvt_pk_bf16_f32 v7, v7, v8
	v_cvt_pk_bf16_f32 v8, v2, v3
	v_fma_f32 v2, v17, v4, v103
	ds_read_b128 v[10:13], v139 offset:16384
	v_fma_f32 v3, v54, v5, v104
	v_cvt_pk_bf16_f32 v9, v2, v3
	ds_read_b128 v[2:5], v139 offset:16400
	global_store_dwordx4 v146, v[6:9], s[26:27]
	s_waitcnt lgkmcnt(0)
	v_fma_f32 v2, v16, v2, v101
	v_fma_f32 v6, v14, v10, v93
	v_fma_f32 v7, v94, v11, v98
	v_cvt_pk_bf16_f32 v6, v6, v7
	v_fma_f32 v7, v15, v12, v99
	v_fma_f32 v8, v95, v13, v100
	v_fma_f32 v3, v96, v3, v102
	v_cvt_pk_bf16_f32 v7, v7, v8
	v_cvt_pk_bf16_f32 v8, v2, v3
	v_fma_f32 v2, v17, v4, v103
	v_fma_f32 v3, v54, v5, v104
	ds_read_b128 v[10:13], v139 offset:24576
	v_cvt_pk_bf16_f32 v9, v2, v3
	ds_read_b128 v[2:5], v139 offset:24592
	global_store_dwordx4 v146, v[6:9], s[24:25]
	s_waitcnt lgkmcnt(1)
	v_fmac_f32_e32 v93, v14, v10
	v_fmac_f32_e32 v98, v94, v11
	v_fmac_f32_e32 v99, v15, v12
	v_fmac_f32_e32 v100, v95, v13
	s_waitcnt lgkmcnt(0)
	v_fmac_f32_e32 v101, v16, v2
	v_fmac_f32_e32 v102, v96, v3
	v_fmac_f32_e32 v103, v17, v4
	v_fmac_f32_e32 v104, v54, v5
	v_cvt_pk_bf16_f32 v6, v93, v98
	v_cvt_pk_bf16_f32 v7, v99, v100
	v_cvt_pk_bf16_f32 v8, v101, v102
	v_cvt_pk_bf16_f32 v9, v103, v104
	global_store_dwordx4 v146, v[6:9], s[22:23]
	s_add_i32 s3, s3, -1
	s_add_i32 s43, s43, 16
	s_add_i32 s48, s48, 0x8000
	s_add_i32 s36, s36, 8
	s_add_i32 s45, s45, 8
	s_cmp_eq_u32 s3, 0
	s_mov_b32 s26, s49
	s_waitcnt vmcnt(34)
	v_mov_b64_e32 v[90:91], v[72:73]
	s_waitcnt vmcnt(33)
	v_mov_b64_e32 v[16:17], v[74:75]
	s_waitcnt vmcnt(32)
	v_mov_b64_e32 v[14:15], v[76:77]
	s_waitcnt vmcnt(31)
	v_mov_b64_e32 v[12:13], v[78:79]
	s_waitcnt vmcnt(30)
	v_mov_b64_e32 v[10:11], v[80:81]
	s_waitcnt vmcnt(29)
	v_mov_b64_e32 v[8:9], v[82:83]
	s_waitcnt vmcnt(28)
	v_mov_b64_e32 v[6:7], v[84:85]
	s_waitcnt vmcnt(27)
	v_mov_b64_e32 v[4:5], v[86:87]
	s_waitcnt vmcnt(24)
	v_mov_b32_e32 v2, v148
	v_mov_b32_e32 v3, v147
	s_cbranch_scc1 .LBB0_1155
	s_branch .LBB0_1140
